# adds: converted expert weights stored non-temporal
# speedup vs baseline: 1.0180x; 1.0102x over previous
.Lcvda_go:
	v_add_u32_e32 v89, s72, v84
	v_add_u32_e32 v90, 1040, v89
	ds_read2_b32 v[4:5], v89 offset0:0 offset1:32
	ds_read2_b32 v[6:7], v89 offset0:64 offset1:96
	ds_read2_b32 v[8:9], v89 offset0:128 offset1:160
	ds_read2_b32 v[10:11], v89 offset0:192 offset1:224
	ds_read2_b32 v[12:13], v90 offset0:0 offset1:32
	ds_read2_b32 v[14:15], v90 offset0:64 offset1:96
	ds_read2_b32 v[16:17], v90 offset0:128 offset1:160
	ds_read2_b32 v[18:19], v90 offset0:192 offset1:224
	ds_read2_b32 v[20:21], v89 offset0:16 offset1:48
	ds_read2_b32 v[22:23], v89 offset0:80 offset1:112
	ds_read2_b32 v[24:25], v89 offset0:144 offset1:176
	ds_read2_b32 v[26:27], v89 offset0:208 offset1:240
	ds_read2_b32 v[28:29], v90 offset0:16 offset1:48
	ds_read2_b32 v[30:31], v90 offset0:80 offset1:112
	ds_read2_b32 v[32:33], v90 offset0:144 offset1:176
	ds_read2_b32 v[34:35], v90 offset0:208 offset1:240
	s_cmp_eq_u32 s98, 0
	s_cselect_b64 vcc, -1, 0
	s_movk_i32 s7, 0x2000
	s_cselect_b32 s7, 0x8000, s7
	v_cndmask_b32_e32 v91, v87, v86, vcc
	s_waitcnt lgkmcnt(8)
	v_pk_mul_f32 v[4:5], v[4:5], v[100:101]
	v_pk_mul_f32 v[6:7], v[6:7], v[100:101]
	v_pk_mul_f32 v[8:9], v[8:9], v[100:101]
	v_pk_mul_f32 v[10:11], v[10:11], v[100:101]
	v_pk_mul_f32 v[12:13], v[12:13], v[100:101]
	v_pk_mul_f32 v[14:15], v[14:15], v[100:101]
	v_pk_mul_f32 v[16:17], v[16:17], v[100:101]
	v_pk_mul_f32 v[18:19], v[18:19], v[100:101]
	v_cvt_pk_fp8_f32 v92, v4, v5
	v_cvt_pk_fp8_f32 v93, v8, v9
	v_cvt_pk_fp8_f32 v94, v12, v13
	v_cvt_pk_fp8_f32 v95, v16, v17
	v_cvt_pk_fp8_f32 v92, v6, v7 op_sel:[0,0,1]
	v_cvt_pk_fp8_f32 v93, v10, v11 op_sel:[0,0,1]
	v_cvt_pk_fp8_f32 v94, v14, v15 op_sel:[0,0,1]
	v_cvt_pk_fp8_f32 v95, v18, v19 op_sel:[0,0,1]
	global_store_dwordx4 v91, v[92:95], s[84:85] nt
	s_waitcnt lgkmcnt(0)
	v_pk_mul_f32 v[20:21], v[20:21], v[100:101]
	v_pk_mul_f32 v[22:23], v[22:23], v[100:101]
	v_pk_mul_f32 v[24:25], v[24:25], v[100:101]
	v_pk_mul_f32 v[26:27], v[26:27], v[100:101]
	v_pk_mul_f32 v[28:29], v[28:29], v[100:101]
	v_pk_mul_f32 v[30:31], v[30:31], v[100:101]
	v_pk_mul_f32 v[32:33], v[32:33], v[100:101]
	v_pk_mul_f32 v[34:35], v[34:35], v[100:101]
	v_cvt_pk_fp8_f32 v96, v20, v21
	v_cvt_pk_fp8_f32 v97, v24, v25
	v_cvt_pk_fp8_f32 v98, v28, v29
	v_cvt_pk_fp8_f32 v99, v32, v33
	v_cvt_pk_fp8_f32 v96, v22, v23 op_sel:[0,0,1]
	v_cvt_pk_fp8_f32 v97, v26, v27 op_sel:[0,0,1]
	v_cvt_pk_fp8_f32 v98, v30, v31 op_sel:[0,0,1]
	v_cvt_pk_fp8_f32 v99, v34, v35 op_sel:[0,0,1]
	s_add_u32 s84, s84, s7
	s_addc_u32 s85, s85, 0
	global_store_dwordx4 v91, v[96:99], s[84:85] nt
	s_mov_b32 s32, 1
	s_cmp_eq_u32 s13, 0
	s_cbranch_scc1 .LBB0_1759
	s_mov_b32 s25, s12
	s_mov_b32 s7, s72
	s_mov_b32 s72, s86
	s_mov_b32 s86, s7
	s_branch .Lcvda_loop
